# hgrn_combine: loop-invariant group-norm weight vector loaded once before the loop (was 8 serialized reloads per trip behind vmcnt(0)); counted waits
# speedup vs baseline: 1.0097x; 1.0021x over previous
.LBB0_3171:
	s_cmp_gt_i32 s6, 53
	s_cselect_b64 s[0:1], -1, 0
	s_cmp_lt_i32 s7, 54
	s_cselect_b64 s[2:3], -1, 0
	s_or_b64 s[0:1], s[0:1], s[2:3]
	s_and_b64 vcc, exec, s[0:1]
	s_cbranch_vccnz .LBB0_3225
	s_lshl_b32 s0, s88, 3
	v_readlane_b32 s1, v253, 20
	s_add_i32 s2, s0, s1
	s_cmpk_gt_i32 s2, 0x3fff
	s_waitcnt vmcnt(0)
	v_mbcnt_lo_u32_b32 v0, -1, 0
	v_mbcnt_hi_u32_b32 v0, -1, v0
	s_cbranch_scc1 .LBB0_3175
	v_lshlrev_b32_e32 v44, 2, v0
	v_ashrrev_i32_e32 v45, 31, v44
	s_add_u32 s18, s94, 0x47600000
	v_lshlrev_b64 v[2:3], 1, v[44:45]
	s_addc_u32 s19, s95, 0
	v_lshl_add_u64 v[4:5], s[94:95], 0, v[2:3]
	s_mov_b64 s[0:1], 0x4f600000
	s_ashr_i32 s3, s2, 31
	v_lshl_add_u64 v[48:49], v[4:5], 0, s[0:1]
	s_lshl_b64 s[0:1], s[2:3], 11
	v_mov_b32_e32 v4, 0x2800
	s_lshl_b32 s4, s90, 4
	v_readlane_b32 s36, v253, 4
	v_lshl_add_u64 v[50:51], s[0:1], 0, v[2:3]
	v_mad_i64_i32 v[52:53], s[0:1], s2, v4, v[2:3]
	v_lshlrev_b64 v[0:1], 2, v[44:45]
	v_readlane_b32 s37, v253, 5
	s_ashr_i32 s5, s4, 31
	s_lshl_b64 s[0:1], s[2:3], 12
	s_lshl_b32 s20, s90, 3
	v_lshl_add_u64 v[46:47], s[36:37], 0, v[0:1]
	s_nop 1
	global_load_dwordx4 v[200:203], v[46:47], off
	global_load_dwordx4 v[204:207], v[46:47], off offset:1024
	global_load_dwordx4 v[208:211], v[46:47], off offset:2048
	global_load_dwordx4 v[212:215], v[46:47], off offset:3072
	s_lshl_b64 s[6:7], s[4:5], 11
	s_mul_i32 s8, s90, 0x28000
	s_mul_hi_i32 s9, s4, 0x2800
	v_lshl_add_u64 v[54:55], s[0:1], 0, v[0:1]
	s_lshl_b64 s[10:11], s[4:5], 12
	s_mov_b32 s3, 0x3d602000
	s_mov_b64 s[12:13], 0x4000000
	s_brev_b32 s5, 32
	s_mov_b64 s[14:15], 0x3d602000
	v_mov_b32_e32 v68, 0x358637bd
	s_mov_b32 s21, 0x4f600000
	v_readlane_b32 s38, v253, 6
	v_readlane_b32 s39, v253, 7
	v_readlane_b32 s40, v253, 8
	v_readlane_b32 s41, v253, 9
	v_readlane_b32 s42, v253, 10
	v_readlane_b32 s43, v253, 11
	v_readlane_b32 s44, v253, 12
	v_readlane_b32 s45, v253, 13
	v_readlane_b32 s46, v253, 14
	v_readlane_b32 s47, v253, 15
	v_readlane_b32 s48, v253, 16
	v_readlane_b32 s49, v253, 17
	v_readlane_b32 s50, v253, 18
	v_readlane_b32 s51, v253, 19
	s_waitcnt vmcnt(0)
.LBB0_3174:
	v_lshl_add_u64 v[0:1], s[94:95], 0, v[54:55]
	v_add_co_u32_e32 v6, vcc, 0x47600000, v0
	v_mov_b32_e32 v40, v200
	v_mov_b32_e32 v41, v201
	v_mov_b32_e32 v42, v202
	v_mov_b32_e32 v43, v203
	s_nop 0
	v_addc_co_u32_e32 v7, vcc, 0, v1, vcc
	v_add_co_u32_e32 v0, vcc, 0x4b600000, v0
	v_lshl_add_u64 v[2:3], s[94:95], 0, v[52:53]
	s_nop 0
	v_addc_co_u32_e32 v1, vcc, 0, v1, vcc
	global_load_dwordx4 v[70:73], v[6:7], off
	global_load_dwordx4 v[74:77], v[6:7], off offset:1024
	global_load_dwordx4 v[78:81], v[6:7], off offset:2048
	global_load_dwordx4 v[32:35], v[6:7], off offset:3072
	global_load_dwordx4 v[82:85], v[0:1], off
	global_load_dwordx4 v[86:89], v[0:1], off offset:1024
	global_load_dwordx4 v[90:93], v[0:1], off offset:2048
	v_add_co_u32_e32 v2, vcc, 0x3d602000, v2
	global_load_dwordx4 v[36:39], v[0:1], off offset:3072
	s_nop 0
	v_addc_co_u32_e32 v3, vcc, 0, v3, vcc
	global_load_dwordx2 v[94:95], v[2:3], off
	global_load_dwordx2 v[96:97], v[2:3], off offset:512
	global_load_dwordx2 v[98:99], v[2:3], off offset:1024
	global_load_dwordx2 v[66:67], v[2:3], off offset:1536
	v_lshl_add_u64 v[4:5], s[94:95], 0, v[50:51]
	s_add_i32 s16, s20, s2
	v_add_co_u32_e64 v64, s[0:1], s21, v4
	s_ashr_i32 s17, s16, 31
	s_nop 0
	v_addc_co_u32_e64 v65, s[0:1], 0, v5, s[0:1]
	s_lshl_b64 s[0:1], s[16:17], 12
	s_add_u32 s0, s18, s0
	s_mul_i32 s22, s16, 0x2800
	s_addc_u32 s1, s19, s1
	s_mul_hi_i32 s23, s16, 0x2800
	s_add_u32 s22, s94, s22
	v_lshl_add_u64 v[0:1], v[44:45], 2, s[0:1]
	s_addc_u32 s23, s95, s23
	v_add_co_u32_e32 v6, vcc, s5, v0
	v_lshl_add_u64 v[56:57], v[44:45], 1, s[22:23]
	s_nop 0
	v_addc_co_u32_e32 v7, vcc, 0, v1, vcc
	v_lshl_add_u64 v[100:101], v[56:57], 0, s[14:15]
	v_add_co_u32_e32 v56, vcc, s3, v56
	v_lshl_add_u64 v[4:5], v[0:1], 0, s[12:13]
	s_nop 0
	v_addc_co_u32_e32 v57, vcc, 0, v57, vcc
	global_load_dwordx4 v[24:27], v[0:1], off
	global_load_dwordx4 v[16:19], v[0:1], off offset:1024
	global_load_dwordx4 v[8:11], v[0:1], off offset:2048
	s_nop 0
	global_load_dwordx4 v[0:3], v[0:1], off offset:3072
	s_nop 0
	global_load_dwordx4 v[20:23], v[4:5], off offset:1024
	global_load_dwordx4 v[12:15], v[4:5], off offset:2048
	global_load_dwordx4 v[28:31], v[6:7], off
	s_nop 0
	global_load_dwordx4 v[4:7], v[4:5], off offset:3072
	s_nop 0
	global_load_dwordx2 v[62:63], v[56:57], off
	global_load_dwordx2 v[60:61], v[100:101], off offset:512
	global_load_dwordx2 v[58:59], v[100:101], off offset:1024
	s_nop 0
	global_load_dwordx2 v[56:57], v[100:101], off offset:1536
	s_lshl_b64 s[0:1], s[16:17], 11
	s_add_i32 s2, s2, s4
	v_lshl_add_u64 v[50:51], v[50:51], 0, s[6:7]
	v_lshl_add_u64 v[52:53], v[52:53], 0, s[8:9]
	v_lshl_add_u64 v[54:55], v[54:55], 0, s[10:11]
	s_cmpk_lt_i32 s2, 0x4000
	s_nop 0
	v_mov_b32_e32 v101, v40
	v_mov_b32_e32 v103, v42
	s_waitcnt vmcnt(19)
	v_pk_add_f32 v[72:73], v[72:73], v[84:85]
	v_pk_add_f32 v[70:71], v[70:71], v[82:83]
	v_mul_f32_e32 v42, v73, v73
	v_mul_f32_e32 v40, v71, v71
	s_waitcnt vmcnt(18)
	v_pk_add_f32 v[76:77], v[76:77], v[88:89]
	v_pk_add_f32 v[74:75], v[74:75], v[86:87]
	s_waitcnt vmcnt(15)
	v_lshlrev_b32_e32 v82, 16, v94
	v_and_b32_e32 v84, 0xffff0000, v94
	v_lshlrev_b32_e32 v86, 16, v95
	v_and_b32_e32 v88, 0xffff0000, v95
	v_fmac_f32_e32 v40, v70, v70
	v_fmac_f32_e32 v42, v72, v72
	v_mul_f32_e32 v83, 0xbfb8aa3b, v82
	v_mul_f32_e32 v85, 0xbfb8aa3b, v84
	v_mul_f32_e32 v87, 0xbfb8aa3b, v86
	v_mul_f32_e32 v89, 0xbfb8aa3b, v88
	v_add_f32_e32 v40, v40, v42
	v_exp_f32_e32 v42, v83
	v_exp_f32_e32 v83, v85
	v_exp_f32_e32 v85, v87
	v_exp_f32_e32 v87, v89
	v_add_f32_dpp v40, v40, v40 quad_perm:[1,0,3,2] row_mask:0xf bank_mask:0xf bound_ctrl:1
	v_pk_add_f32 v[78:79], v[78:79], v[90:91]
	v_mul_f32_e32 v69, v75, v75
	v_add_f32_dpp v40, v40, v40 quad_perm:[2,3,0,1] row_mask:0xf bank_mask:0xf bound_ctrl:1
	v_mul_f32_e32 v91, v77, v77
	v_pk_add_f32 v[80:81], v[80:81], v[92:93]
	v_add_f32_dpp v40, v40, v40 row_half_mirror row_mask:0xf bank_mask:0xf bound_ctrl:1
	s_waitcnt vmcnt(14)
	v_lshlrev_b32_e32 v90, 16, v96
	v_and_b32_e32 v92, 0xffff0000, v96
	v_add_f32_dpp v89, v40, v40 row_mirror row_mask:0xf bank_mask:0xf bound_ctrl:1
	v_add_f32_e32 v40, 1.0, v42
	v_add_f32_e32 v42, 1.0, v83
	v_add_f32_e32 v83, 1.0, v85
	v_add_f32_e32 v85, 1.0, v87
	v_mov_b32_e32 v87, v89
	s_nop 1
	v_permlane16_swap_b32_e32 v89, v87
	v_rcp_f32_e32 v102, v83
	v_add_f32_e32 v83, v89, v87
	v_fmamk_f32 v83, v83, 0x3c000000, v68
	v_rsq_f32_e32 v89, v83
	v_rcp_f32_e32 v100, v40
	v_rcp_f32_e32 v40, v42
	v_rcp_f32_e32 v42, v85
	v_mul_f32_e32 v85, v71, v89
	v_mul_f32_e32 v87, v72, v89
	v_mul_f32_e32 v83, v70, v89
	v_mul_f32_e32 v89, v73, v89
	v_pk_mul_f32 v[40:41], v[40:41], v[84:85]
	v_pk_mul_f32 v[72:73], v[102:103], v[86:87]
	v_pk_mul_f32 v[70:71], v[100:101], v[82:83]
	v_pk_mul_f32 v[42:43], v[42:43], v[88:89]
	v_mul_f32_e32 v40, v40, v41
	v_mul_f32_e32 v41, v72, v73
	v_mul_f32_e32 v70, v70, v71
	v_mul_f32_e32 v42, v42, v43
	v_cvt_pk_bf16_f32 v40, v70, v40
	v_cvt_pk_bf16_f32 v41, v41, v42
	global_store_dwordx2 v[64:65], v[40:41], off
	v_mov_b32_e32 v40, v204
	v_mov_b32_e32 v41, v205
	v_mov_b32_e32 v42, v206
	v_mov_b32_e32 v43, v207
	v_and_b32_e32 v96, 0xffff0000, v97
	v_fmac_f32_e32 v69, v74, v74
	v_fmac_f32_e32 v91, v76, v76
	v_mul_f32_e32 v71, 0xbfb8aa3b, v96
	v_add_f32_e32 v69, v69, v91
	v_exp_f32_e32 v71, v71
	v_lshlrev_b32_e32 v94, 16, v97
	v_add_f32_dpp v69, v69, v69 quad_perm:[1,0,3,2] row_mask:0xf bank_mask:0xf bound_ctrl:1
	v_mul_f32_e32 v95, 0xbfb8aa3b, v92
	v_mul_f32_e32 v93, 0xbfb8aa3b, v90
	v_add_f32_dpp v69, v69, v69 quad_perm:[2,3,0,1] row_mask:0xf bank_mask:0xf bound_ctrl:1
	v_mul_f32_e32 v70, 0xbfb8aa3b, v94
	v_exp_f32_e32 v73, v95
	v_add_f32_dpp v69, v69, v69 row_half_mirror row_mask:0xf bank_mask:0xf bound_ctrl:1
	v_add_f32_e32 v83, 1.0, v71
	v_exp_f32_e32 v72, v93
	v_add_f32_dpp v69, v69, v69 row_mirror row_mask:0xf bank_mask:0xf bound_ctrl:1
	v_mov_b32_e32 v71, v69
	v_exp_f32_e32 v70, v70
	s_nop 0
	v_permlane16_swap_b32_e32 v69, v71
	v_add_f32_e32 v69, v69, v71
	v_fmamk_f32 v69, v69, 0x3c000000, v68
	v_add_f32_e32 v73, 1.0, v73
	v_rsq_f32_e32 v69, v69
	v_add_f32_e32 v72, 1.0, v72
	v_add_f32_e32 v82, 1.0, v70
	v_rcp_f32_e32 v70, v72
	v_rcp_f32_e32 v72, v82
	v_mul_f32_e32 v93, v75, v69
	v_mul_f32_e32 v97, v77, v69
	v_mul_f32_e32 v91, v74, v69
	v_mul_f32_e32 v95, v76, v69
	v_mul_f32_e32 v105, v79, v79
	v_mul_f32_e32 v106, v81, v81
	v_fmac_f32_e32 v105, v78, v78
	v_fmac_f32_e32 v106, v80, v80
	s_waitcnt vmcnt(14)
	v_lshlrev_b32_e32 v104, 16, v98
	v_add_f32_e32 v76, v105, v106
	v_and_b32_e32 v74, 0xffff0000, v99
	v_mul_f32_e32 v75, 0xbfb8aa3b, v74
	v_add_f32_dpp v76, v76, v76 quad_perm:[1,0,3,2] row_mask:0xf bank_mask:0xf bound_ctrl:1
	v_exp_f32_e32 v75, v75
	v_pk_add_f32 v[34:35], v[34:35], v[38:39]
	v_add_f32_dpp v76, v76, v76 quad_perm:[2,3,0,1] row_mask:0xf bank_mask:0xf bound_ctrl:1
	v_pk_add_f32 v[32:33], v[32:33], v[36:37]
	v_add_f32_e32 v84, 1.0, v75
	v_add_f32_dpp v76, v76, v76 row_half_mirror row_mask:0xf bank_mask:0xf bound_ctrl:1
	v_mul_f32_e32 v37, v33, v33
	v_mul_f32_e32 v39, v35, v35
	v_add_f32_dpp v77, v76, v76 row_mirror row_mask:0xf bank_mask:0xf bound_ctrl:1
	s_waitcnt vmcnt(13)
	v_lshlrev_b32_e32 v36, 16, v66
	v_and_b32_e32 v38, 0xffff0000, v66
	v_lshlrev_b32_e32 v66, 16, v67
	v_fmac_f32_e32 v37, v32, v32
	v_fmac_f32_e32 v39, v34, v34
	v_add_f32_e32 v37, v37, v39
	s_waitcnt vmcnt(6)
	v_pk_add_f32 v[26:27], v[26:27], v[30:31]
	v_pk_add_f32 v[24:25], v[24:25], v[28:29]
	v_add_f32_dpp v37, v37, v37 quad_perm:[1,0,3,2] row_mask:0xf bank_mask:0xf bound_ctrl:1
	v_mul_f32_e32 v29, v25, v25
	v_mul_f32_e32 v31, v27, v27
	v_add_f32_dpp v37, v37, v37 quad_perm:[2,3,0,1] row_mask:0xf bank_mask:0xf bound_ctrl:1
	v_fmac_f32_e32 v29, v24, v24
	v_fmac_f32_e32 v31, v26, v26
	v_add_f32_dpp v37, v37, v37 row_half_mirror row_mask:0xf bank_mask:0xf bound_ctrl:1
	v_add_f32_e32 v29, v29, v31
	s_waitcnt vmcnt(4)
	v_lshlrev_b32_e32 v28, 16, v62
	v_add_f32_dpp v37, v37, v37 row_mirror row_mask:0xf bank_mask:0xf bound_ctrl:1
	v_add_f32_dpp v29, v29, v29 quad_perm:[1,0,3,2] row_mask:0xf bank_mask:0xf bound_ctrl:1
	v_and_b32_e32 v30, 0xffff0000, v62
	v_mul_f32_e32 v31, 0xbfb8aa3b, v28
	v_add_f32_dpp v29, v29, v29 quad_perm:[2,3,0,1] row_mask:0xf bank_mask:0xf bound_ctrl:1
	v_exp_f32_e32 v31, v31
	v_pk_add_f32 v[18:19], v[18:19], v[22:23]
	v_add_f32_dpp v29, v29, v29 row_half_mirror row_mask:0xf bank_mask:0xf bound_ctrl:1
	v_pk_add_f32 v[16:17], v[16:17], v[20:21]
	v_add_f32_e32 v31, 1.0, v31
	v_add_f32_dpp v29, v29, v29 row_mirror row_mask:0xf bank_mask:0xf bound_ctrl:1
	s_waitcnt vmcnt(1)
	v_mov_b32_e32 v71, v40
	v_rcp_f32_e32 v40, v73
	v_mov_b32_e32 v73, v42
	v_rcp_f32_e32 v42, v83
	v_pk_mul_f32 v[70:71], v[70:71], v[90:91]
	v_pk_mul_f32 v[40:41], v[40:41], v[92:93]
	v_pk_mul_f32 v[72:73], v[72:73], v[94:95]
	v_pk_mul_f32 v[42:43], v[42:43], v[96:97]
	v_mul_f32_e32 v40, v40, v41
	v_mul_f32_e32 v41, v42, v43
	v_mul_f32_e32 v69, v70, v71
	v_mul_f32_e32 v70, v72, v73
	v_cvt_pk_bf16_f32 v40, v69, v40
	v_cvt_pk_bf16_f32 v41, v70, v41
	global_store_dwordx2 v[64:65], v[40:41], off offset:512
	v_mov_b32_e32 v40, v208
	v_mov_b32_e32 v41, v209
	v_mov_b32_e32 v42, v210
	v_mov_b32_e32 v43, v211
	v_and_b32_e32 v70, 0xffff0000, v98
	v_lshlrev_b32_e32 v72, 16, v99
	v_mul_f32_e32 v71, 0xbfb8aa3b, v70
	v_mul_f32_e32 v73, 0xbfb8aa3b, v72
	v_mul_f32_e32 v69, 0xbfb8aa3b, v104
	v_exp_f32_e32 v71, v71
	v_exp_f32_e32 v73, v73
	v_exp_f32_e32 v69, v69
	v_mul_f32_e32 v21, v17, v17
	v_add_f32_e32 v83, 1.0, v71
	v_add_f32_e32 v71, 1.0, v73
	v_mov_b32_e32 v73, v77
	v_add_f32_e32 v69, 1.0, v69
	s_nop 0
	v_permlane16_swap_b32_e32 v77, v73
	v_rcp_f32_e32 v76, v69
	v_add_f32_e32 v69, v77, v73
	v_fmamk_f32 v69, v69, 0x3c000000, v68
	v_rsq_f32_e32 v69, v69
	v_rcp_f32_e32 v82, v71
	v_mul_f32_e32 v23, v19, v19
	v_fmac_f32_e32 v21, v16, v16
	v_mul_f32_e32 v71, v79, v69
	v_mul_f32_e32 v75, v81, v69
	v_mul_f32_e32 v105, v78, v69
	v_mul_f32_e32 v73, v80, v69
	v_fmac_f32_e32 v23, v18, v18
	v_add_f32_e32 v21, v21, v23
	v_lshlrev_b32_e32 v20, 16, v60
	v_and_b32_e32 v22, 0xffff0000, v60
	v_add_f32_dpp v21, v21, v21 quad_perm:[1,0,3,2] row_mask:0xf bank_mask:0xf bound_ctrl:1
	v_mul_f32_e32 v23, 0xbfb8aa3b, v20
	v_exp_f32_e32 v23, v23
	v_add_f32_dpp v21, v21, v21 quad_perm:[2,3,0,1] row_mask:0xf bank_mask:0xf bound_ctrl:1
	v_pk_add_f32 v[10:11], v[10:11], v[14:15]
	v_pk_add_f32 v[8:9], v[8:9], v[12:13]
	v_add_f32_dpp v21, v21, v21 row_half_mirror row_mask:0xf bank_mask:0xf bound_ctrl:1
	v_add_f32_e32 v23, 1.0, v23
	v_mul_f32_e32 v13, v9, v9
	v_add_f32_dpp v21, v21, v21 row_mirror row_mask:0xf bank_mask:0xf bound_ctrl:1
	v_mul_f32_e32 v15, v11, v11
	v_fmac_f32_e32 v13, v8, v8
	v_fmac_f32_e32 v15, v10, v10
	v_add_f32_e32 v13, v13, v15
	v_lshlrev_b32_e32 v12, 16, v58
	v_and_b32_e32 v14, 0xffff0000, v58
	v_add_f32_dpp v13, v13, v13 quad_perm:[1,0,3,2] row_mask:0xf bank_mask:0xf bound_ctrl:1
	v_mul_f32_e32 v15, 0xbfb8aa3b, v12
	v_exp_f32_e32 v15, v15
	v_add_f32_dpp v13, v13, v13 quad_perm:[2,3,0,1] row_mask:0xf bank_mask:0xf bound_ctrl:1
	v_pk_add_f32 v[2:3], v[2:3], v[6:7]
	v_pk_add_f32 v[0:1], v[0:1], v[4:5]
	v_add_f32_dpp v13, v13, v13 row_half_mirror row_mask:0xf bank_mask:0xf bound_ctrl:1
	v_add_f32_e32 v15, 1.0, v15
	v_mul_f32_e32 v5, v1, v1
	v_add_f32_dpp v13, v13, v13 row_mirror row_mask:0xf bank_mask:0xf bound_ctrl:1
	v_mul_f32_e32 v7, v3, v3
	v_fmac_f32_e32 v5, v0, v0
	v_fmac_f32_e32 v7, v2, v2
	v_add_f32_e32 v5, v5, v7
	v_lshlrev_b32_e32 v4, 16, v56
	v_and_b32_e32 v6, 0xffff0000, v56
	v_add_f32_dpp v5, v5, v5 quad_perm:[1,0,3,2] row_mask:0xf bank_mask:0xf bound_ctrl:1
	v_mul_f32_e32 v7, 0xbfb8aa3b, v4
	v_exp_f32_e32 v7, v7
	v_add_f32_dpp v5, v5, v5 quad_perm:[2,3,0,1] row_mask:0xf bank_mask:0xf bound_ctrl:1
	v_add_f32_e32 v7, 1.0, v7
	s_nop 0
	v_add_f32_dpp v5, v5, v5 row_half_mirror row_mask:0xf bank_mask:0xf bound_ctrl:1
	s_nop 0
	v_mov_b32_e32 v77, v40
	v_rcp_f32_e32 v40, v83
	v_mov_b32_e32 v83, v42
	v_rcp_f32_e32 v42, v84
	v_pk_mul_f32 v[76:77], v[76:77], v[104:105]
	v_pk_mul_f32 v[40:41], v[40:41], v[70:71]
	v_pk_mul_f32 v[72:73], v[82:83], v[72:73]
	v_pk_mul_f32 v[42:43], v[42:43], v[74:75]
	v_mul_f32_e32 v40, v40, v41
	v_mul_f32_e32 v41, v42, v43
	v_mul_f32_e32 v69, v76, v77
	v_mul_f32_e32 v72, v72, v73
	v_cvt_pk_bf16_f32 v40, v69, v40
	v_cvt_pk_bf16_f32 v41, v72, v41
	global_store_dwordx2 v[64:65], v[40:41], off offset:1024
	v_mov_b32_e32 v40, v212
	v_mov_b32_e32 v41, v213
	v_mov_b32_e32 v42, v214
	v_mov_b32_e32 v43, v215
	v_and_b32_e32 v70, 0xffff0000, v67
	v_mul_f32_e32 v67, 0xbfb8aa3b, v36
	v_mul_f32_e32 v69, 0xbfb8aa3b, v38
	v_mul_f32_e32 v71, 0xbfb8aa3b, v66
	v_mul_f32_e32 v72, 0xbfb8aa3b, v70
	v_exp_f32_e32 v39, v67
	v_exp_f32_e32 v67, v69
	v_exp_f32_e32 v69, v71
	v_exp_f32_e32 v71, v72
	v_add_f32_e32 v39, 1.0, v39
	v_add_f32_e32 v75, 1.0, v67
	v_add_f32_e32 v67, 1.0, v69
	v_add_f32_e32 v69, 1.0, v71
	v_mov_b32_e32 v71, v37
	s_nop 1
	v_permlane16_swap_b32_e32 v37, v71
	v_add_f32_e32 v37, v37, v71
	v_fmamk_f32 v37, v37, 0x3c000000, v68
	v_rsq_f32_e32 v71, v37
	v_rcp_f32_e32 v72, v39
	v_rcp_f32_e32 v74, v67
	v_add_f32_dpp v5, v5, v5 row_mirror row_mask:0xf bank_mask:0xf bound_ctrl:1
	v_mul_f32_e32 v37, v32, v71
	v_mul_f32_e32 v67, v34, v71
	v_mul_f32_e32 v39, v33, v71
	v_mul_f32_e32 v71, v35, v71
	s_nop 0
	v_mov_b32_e32 v73, v40
	v_rcp_f32_e32 v40, v75
	v_mov_b32_e32 v75, v42
	v_rcp_f32_e32 v42, v69
	v_pk_mul_f32 v[32:33], v[72:73], v[36:37]
	v_pk_mul_f32 v[34:35], v[74:75], v[66:67]
	v_mul_f32_e32 v36, v32, v33
	v_mul_f32_e32 v37, v34, v35
	v_pk_mul_f32 v[32:33], v[40:41], v[38:39]
	v_pk_mul_f32 v[34:35], v[42:43], v[70:71]
	v_mul_f32_e32 v32, v32, v33
	v_mul_f32_e32 v33, v34, v35
	v_cvt_pk_bf16_f32 v32, v36, v32
	v_cvt_pk_bf16_f32 v33, v37, v33
	global_store_dwordx2 v[64:65], v[32:33], off offset:1536
	v_mov_b32_e32 v34, v200
	v_mov_b32_e32 v35, v201
	v_mov_b32_e32 v36, v202
	v_mov_b32_e32 v37, v203
	v_lshlrev_b32_e32 v38, 16, v63
	v_and_b32_e32 v40, 0xffff0000, v63
	v_mul_f32_e32 v39, 0xbfb8aa3b, v30
	v_mul_f32_e32 v41, 0xbfb8aa3b, v38
	v_mul_f32_e32 v42, 0xbfb8aa3b, v40
	v_exp_f32_e32 v39, v39
	v_exp_f32_e32 v41, v41
	v_mov_b32_e32 v43, v29
	v_exp_f32_e32 v42, v42
	s_nop 0
	v_permlane16_swap_b32_e32 v29, v43
	v_add_f32_e32 v29, v29, v43
	v_fmamk_f32 v29, v29, 0x3c000000, v68
	v_add_f32_e32 v63, 1.0, v39
	v_add_f32_e32 v39, 1.0, v41
	v_rsq_f32_e32 v41, v29
	v_add_f32_e32 v64, 1.0, v42
	v_rcp_f32_e32 v42, v31
	v_rcp_f32_e32 v62, v39
	v_mul_f32_e32 v29, v24, v41
	v_mul_f32_e32 v39, v26, v41
	v_mul_f32_e32 v31, v25, v41
	v_mul_f32_e32 v41, v27, v41
	v_lshl_add_u64 v[32:33], v[48:49], 0, s[0:1]
	s_nop 0
	v_mov_b32_e32 v43, v34
	v_rcp_f32_e32 v34, v63
	v_mov_b32_e32 v63, v36
	v_rcp_f32_e32 v36, v64
	v_pk_mul_f32 v[24:25], v[42:43], v[28:29]
	v_pk_mul_f32 v[26:27], v[62:63], v[38:39]
	v_mul_f32_e32 v28, v24, v25
	v_mul_f32_e32 v29, v26, v27
	v_pk_mul_f32 v[24:25], v[34:35], v[30:31]
	v_pk_mul_f32 v[26:27], v[36:37], v[40:41]
	v_mul_f32_e32 v24, v24, v25
	v_mul_f32_e32 v25, v26, v27
	v_cvt_pk_bf16_f32 v24, v28, v24
	v_cvt_pk_bf16_f32 v25, v29, v25
	global_store_dwordx2 v[32:33], v[24:25], off
	v_mov_b32_e32 v24, v204
	v_mov_b32_e32 v25, v205
	v_mov_b32_e32 v26, v206
	v_mov_b32_e32 v27, v207
	v_lshlrev_b32_e32 v28, 16, v61
	v_and_b32_e32 v30, 0xffff0000, v61
	v_mul_f32_e32 v29, 0xbfb8aa3b, v22
	v_mul_f32_e32 v31, 0xbfb8aa3b, v28
	v_mul_f32_e32 v34, 0xbfb8aa3b, v30
	v_exp_f32_e32 v29, v29
	v_exp_f32_e32 v31, v31
	v_mov_b32_e32 v35, v21
	v_exp_f32_e32 v34, v34
	s_nop 0
	v_permlane16_swap_b32_e32 v21, v35
	v_add_f32_e32 v21, v21, v35
	v_fmamk_f32 v21, v21, 0x3c000000, v68
	v_add_f32_e32 v37, 1.0, v29
	v_add_f32_e32 v29, 1.0, v31
	v_rsq_f32_e32 v31, v21
	v_add_f32_e32 v38, 1.0, v34
	v_rcp_f32_e32 v34, v23
	v_rcp_f32_e32 v36, v29
	v_mul_f32_e32 v21, v16, v31
	v_mul_f32_e32 v29, v18, v31
	v_mul_f32_e32 v23, v17, v31
	v_mul_f32_e32 v31, v19, v31
	s_nop 0
	v_mov_b32_e32 v35, v24
	v_rcp_f32_e32 v24, v37
	v_mov_b32_e32 v37, v26
	v_rcp_f32_e32 v26, v38
	v_pk_mul_f32 v[16:17], v[34:35], v[20:21]
	v_pk_mul_f32 v[18:19], v[36:37], v[28:29]
	v_mul_f32_e32 v20, v16, v17
	v_mul_f32_e32 v21, v18, v19
	v_pk_mul_f32 v[16:17], v[24:25], v[22:23]
	v_pk_mul_f32 v[18:19], v[26:27], v[30:31]
	v_mul_f32_e32 v16, v16, v17
	v_mul_f32_e32 v17, v18, v19
	v_cvt_pk_bf16_f32 v16, v20, v16
	v_cvt_pk_bf16_f32 v17, v21, v17
	global_store_dwordx2 v[32:33], v[16:17], off offset:512
	v_mov_b32_e32 v16, v208
	v_mov_b32_e32 v17, v209
	v_mov_b32_e32 v18, v210
	v_mov_b32_e32 v19, v211
	v_lshlrev_b32_e32 v20, 16, v59
	v_and_b32_e32 v22, 0xffff0000, v59
	v_mul_f32_e32 v21, 0xbfb8aa3b, v14
	v_mul_f32_e32 v23, 0xbfb8aa3b, v20
	v_mul_f32_e32 v24, 0xbfb8aa3b, v22
	v_exp_f32_e32 v21, v21
	v_exp_f32_e32 v23, v23
	v_mov_b32_e32 v25, v13
	v_exp_f32_e32 v24, v24
	s_nop 0
	v_permlane16_swap_b32_e32 v13, v25
	v_add_f32_e32 v13, v13, v25
	v_fmamk_f32 v13, v13, 0x3c000000, v68
	v_add_f32_e32 v27, 1.0, v21
	v_add_f32_e32 v21, 1.0, v23
	v_rsq_f32_e32 v23, v13
	v_add_f32_e32 v28, 1.0, v24
	v_rcp_f32_e32 v24, v15
	v_rcp_f32_e32 v26, v21
	v_mul_f32_e32 v13, v8, v23
	v_mul_f32_e32 v21, v10, v23
	v_mul_f32_e32 v15, v9, v23
	v_mul_f32_e32 v23, v11, v23
	s_nop 0
	v_mov_b32_e32 v25, v16
	v_rcp_f32_e32 v16, v27
	v_mov_b32_e32 v27, v18
	v_rcp_f32_e32 v18, v28
	v_pk_mul_f32 v[8:9], v[24:25], v[12:13]
	v_pk_mul_f32 v[10:11], v[26:27], v[20:21]
	v_mul_f32_e32 v12, v8, v9
	v_mul_f32_e32 v13, v10, v11
	v_pk_mul_f32 v[8:9], v[16:17], v[14:15]
	v_pk_mul_f32 v[10:11], v[18:19], v[22:23]
	v_mul_f32_e32 v8, v8, v9
	v_mul_f32_e32 v9, v10, v11
	v_cvt_pk_bf16_f32 v8, v12, v8
	v_cvt_pk_bf16_f32 v9, v13, v9
	global_store_dwordx2 v[32:33], v[8:9], off offset:1024
	v_mov_b32_e32 v8, v212
	v_mov_b32_e32 v9, v213
	v_mov_b32_e32 v10, v214
	v_mov_b32_e32 v11, v215
	v_lshlrev_b32_e32 v12, 16, v57
	v_and_b32_e32 v14, 0xffff0000, v57
	v_mul_f32_e32 v13, 0xbfb8aa3b, v6
	v_mul_f32_e32 v15, 0xbfb8aa3b, v12
	v_mul_f32_e32 v16, 0xbfb8aa3b, v14
	v_exp_f32_e32 v13, v13
	v_exp_f32_e32 v15, v15
	v_mov_b32_e32 v17, v5
	v_exp_f32_e32 v16, v16
	s_nop 0
	v_permlane16_swap_b32_e32 v5, v17
	v_add_f32_e32 v5, v5, v17
	v_fmamk_f32 v5, v5, 0x3c000000, v68
	v_add_f32_e32 v19, 1.0, v13
	v_add_f32_e32 v13, 1.0, v15
	v_rsq_f32_e32 v15, v5
	v_add_f32_e32 v20, 1.0, v16
	v_rcp_f32_e32 v16, v7
	v_rcp_f32_e32 v18, v13
	v_mul_f32_e32 v5, v0, v15
	v_mul_f32_e32 v13, v2, v15
	v_mul_f32_e32 v7, v1, v15
	v_mul_f32_e32 v15, v3, v15
	s_nop 0
	v_mov_b32_e32 v17, v8
	v_rcp_f32_e32 v8, v19
	v_mov_b32_e32 v19, v10
	v_rcp_f32_e32 v10, v20
	v_pk_mul_f32 v[0:1], v[16:17], v[4:5]
	v_pk_mul_f32 v[2:3], v[18:19], v[12:13]
	v_mul_f32_e32 v4, v0, v1
	v_mul_f32_e32 v5, v2, v3
	v_pk_mul_f32 v[0:1], v[8:9], v[6:7]
	v_pk_mul_f32 v[2:3], v[10:11], v[14:15]
	v_mul_f32_e32 v0, v0, v1
	v_mul_f32_e32 v1, v2, v3
	v_cvt_pk_bf16_f32 v0, v4, v0
	v_cvt_pk_bf16_f32 v1, v5, v1
	global_store_dwordx2 v[32:33], v[0:1], off offset:1536
	s_cbranch_scc1 .LBB0_3174
